# speedup vs baseline: 1.0014x; 1.0014x over previous
.Lagg_loop:
	s_waitcnt vmcnt(4)
	s_mov_b32 s24, s0
	s_min_i32 s24, s24, s20
	s_mul_i32 s24, s24, s44
	s_add_i32 s24, s24, s45
	s_lshl_b32 s24, s24, 4
	v_add_u32_e32 v33, s24, v18
	v_cmp_gt_i32_e64 s[28:29], s17, v33
	s_add_i32 s24, s0, 16
	s_min_i32 s24, s24, s20
	s_mul_i32 s24, s24, s44
	s_add_i32 s24, s24, s45
	s_lshl_b32 s24, s24, 4
	s_ashr_i32 s25, s24, 31
	v_cndmask_b32_e64 v31, v59, v30, s[28:29]
	v_lshl_add_u64 v[32:33], s[24:25], 2, v[20:21]
	global_load_dword v30, v[32:33], off
	s_waitcnt vmcnt(4)
	v_ashrrev_i32_e32 v32, 17, v29
	v_mul_i32_i24_e32 v32, 0x140, v32
	v_fma_mix_f32 v33, v2, v22, s23 op_sel_hi:[1,0,0]
	v_fma_mix_f32 v34, v2, v22, s23 op_sel:[1,0,0] op_sel_hi:[1,0,0]
	v_or_b32_e32 v32, v23, v32
	v_fma_mix_f32 v36, v3, v22, s23 op_sel_hi:[1,0,0]
	v_fma_mix_f32 v37, v3, v22, s23 op_sel:[1,0,0] op_sel_hi:[1,0,0]
	v_lshl_add_u32 v33, v34, 16, v33
	ds_add_u32 v32, v33
	v_fma_mix_f32 v33, v4, v22, s23 op_sel_hi:[1,0,0]
	v_fma_mix_f32 v34, v4, v22, s23 op_sel:[1,0,0] op_sel_hi:[1,0,0]
	v_lshl_add_u32 v36, v37, 16, v36
	ds_add_u32 v32, v36 offset:64
	v_fma_mix_f32 v36, v5, v22, s23 op_sel_hi:[1,0,0]
	v_fma_mix_f32 v37, v5, v22, s23 op_sel:[1,0,0] op_sel_hi:[1,0,0]
	v_lshl_add_u32 v33, v34, 16, v33
	ds_add_u32 v32, v33 offset:128
	s_nop 0
	v_lshl_add_u32 v36, v37, 16, v36
	ds_add_u32 v32, v36 offset:192
	v_mov_b32_e32 v29, 0
	s_nop 1
	v_mov_b32_dpp v29, v31 row_newbcast:0 row_mask:0xf bank_mask:0xf
	v_lshlrev_b32_e32 v35, 8, v29
	v_and_or_b32 v35, v35, s22, v24
	s_waitcnt vmcnt(2)
	global_load_dwordx4 v[2:5], v35, s[12:13]
	s_waitcnt vmcnt(4)
	v_ashrrev_i32_e32 v32, 17, v27
	v_mul_i32_i24_e32 v32, 0x140, v32
	v_fma_mix_f32 v33, v6, v22, s23 op_sel_hi:[1,0,0]
	v_fma_mix_f32 v34, v6, v22, s23 op_sel:[1,0,0] op_sel_hi:[1,0,0]
	v_or_b32_e32 v32, v23, v32
	v_fma_mix_f32 v36, v7, v22, s23 op_sel_hi:[1,0,0]
	v_fma_mix_f32 v37, v7, v22, s23 op_sel:[1,0,0] op_sel_hi:[1,0,0]
	v_lshl_add_u32 v33, v34, 16, v33
	ds_add_u32 v32, v33
	v_fma_mix_f32 v33, v8, v22, s23 op_sel_hi:[1,0,0]
	v_fma_mix_f32 v34, v8, v22, s23 op_sel:[1,0,0] op_sel_hi:[1,0,0]
	v_lshl_add_u32 v36, v37, 16, v36
	ds_add_u32 v32, v36 offset:64
	v_fma_mix_f32 v36, v9, v22, s23 op_sel_hi:[1,0,0]
	v_fma_mix_f32 v37, v9, v22, s23 op_sel:[1,0,0] op_sel_hi:[1,0,0]
	v_lshl_add_u32 v33, v34, 16, v33
	ds_add_u32 v32, v33 offset:128
	s_nop 0
	v_lshl_add_u32 v36, v37, 16, v36
	ds_add_u32 v32, v36 offset:192
	v_mov_b32_e32 v27, 0
	s_nop 1
	v_mov_b32_dpp v27, v31 row_newbcast:1 row_mask:0xf bank_mask:0xf
	v_lshlrev_b32_e32 v35, 8, v27
	v_and_or_b32 v35, v35, s22, v24
	s_waitcnt vmcnt(1)
	global_load_dwordx4 v[6:9], v35, s[12:13]
	s_waitcnt vmcnt(4)
	v_ashrrev_i32_e32 v32, 17, v28
	v_mul_i32_i24_e32 v32, 0x140, v32
	v_fma_mix_f32 v33, v10, v22, s23 op_sel_hi:[1,0,0]
	v_fma_mix_f32 v34, v10, v22, s23 op_sel:[1,0,0] op_sel_hi:[1,0,0]
	v_or_b32_e32 v32, v23, v32
	v_fma_mix_f32 v36, v11, v22, s23 op_sel_hi:[1,0,0]
	v_fma_mix_f32 v37, v11, v22, s23 op_sel:[1,0,0] op_sel_hi:[1,0,0]
	v_lshl_add_u32 v33, v34, 16, v33
	ds_add_u32 v32, v33
	v_fma_mix_f32 v33, v12, v22, s23 op_sel_hi:[1,0,0]
	v_fma_mix_f32 v34, v12, v22, s23 op_sel:[1,0,0] op_sel_hi:[1,0,0]
	v_lshl_add_u32 v36, v37, 16, v36
	ds_add_u32 v32, v36 offset:64
	v_fma_mix_f32 v36, v13, v22, s23 op_sel_hi:[1,0,0]
	v_fma_mix_f32 v37, v13, v22, s23 op_sel:[1,0,0] op_sel_hi:[1,0,0]
	v_lshl_add_u32 v33, v34, 16, v33
	ds_add_u32 v32, v33 offset:128
	s_nop 0
	v_lshl_add_u32 v36, v37, 16, v36
	ds_add_u32 v32, v36 offset:192
	v_mov_b32_e32 v28, 0
	s_nop 1
	v_mov_b32_dpp v28, v31 row_newbcast:2 row_mask:0xf bank_mask:0xf
	v_lshlrev_b32_e32 v35, 8, v28
	v_and_or_b32 v35, v35, s22, v24
	s_waitcnt vmcnt(1)
	global_load_dwordx4 v[10:13], v35, s[12:13]
	s_waitcnt vmcnt(4)
	v_ashrrev_i32_e32 v32, 17, v26
	v_mul_i32_i24_e32 v32, 0x140, v32
	v_fma_mix_f32 v33, v14, v22, s23 op_sel_hi:[1,0,0]
	v_fma_mix_f32 v34, v14, v22, s23 op_sel:[1,0,0] op_sel_hi:[1,0,0]
	v_or_b32_e32 v32, v23, v32
	v_fma_mix_f32 v36, v15, v22, s23 op_sel_hi:[1,0,0]
	v_fma_mix_f32 v37, v15, v22, s23 op_sel:[1,0,0] op_sel_hi:[1,0,0]
	v_lshl_add_u32 v33, v34, 16, v33
	ds_add_u32 v32, v33
	v_fma_mix_f32 v33, v16, v22, s23 op_sel_hi:[1,0,0]
	v_fma_mix_f32 v34, v16, v22, s23 op_sel:[1,0,0] op_sel_hi:[1,0,0]
	v_lshl_add_u32 v36, v37, 16, v36
	ds_add_u32 v32, v36 offset:64
	v_fma_mix_f32 v36, v17, v22, s23 op_sel_hi:[1,0,0]
	v_fma_mix_f32 v37, v17, v22, s23 op_sel:[1,0,0] op_sel_hi:[1,0,0]
	v_lshl_add_u32 v33, v34, 16, v33
	ds_add_u32 v32, v33 offset:128
	s_nop 0
	v_lshl_add_u32 v36, v37, 16, v36
	ds_add_u32 v32, v36 offset:192
	v_mov_b32_e32 v26, 0
	s_nop 1
	v_mov_b32_dpp v26, v31 row_newbcast:3 row_mask:0xf bank_mask:0xf
	v_lshlrev_b32_e32 v35, 8, v26
	v_and_or_b32 v35, v35, s22, v24
	s_waitcnt vmcnt(1)
	global_load_dwordx4 v[14:17], v35, s[12:13]
	s_add_i32 s1, s1, 1
	s_add_i32 s0, s0, 16
	s_cmp_lt_u32 s1, s21
	s_cbranch_scc1 .Lagg_loop
